# MoE fused GEMM: XCD-aware workgroup-to-unit permutation (4-column x 8-row blocks per XCD) on top of attention tile rewrite
# speedup vs baseline: 1.0144x; 1.0005x over previous
.LBB0_1360:
	s_andn2_b64 vcc, exec, s[0:1]
	s_cbranch_vccnz .LBB0_1556
	s_and_b32 s0, s95, 7
	s_lshr_b32 s1, s95, 3
	s_lshl_b32 s0, s0, 3
	s_lshr_b32 s2, s1, 2
	s_add_i32 s0, s0, s2
	s_and_b32 s1, s1, 3
	s_sub_i32 s2, s0, 10
	s_mul_i32 s3, s2, 57
	s_lshr_b32 s3, s3, 9
	s_mul_i32 s4, s3, 9
	s_sub_i32 s4, s2, s4
	s_add_i32 s3, s3, 1
	s_cmp_lt_u32 s0, 10
	s_cselect_b32 s3, 0, s3
	s_cselect_b32 s4, s0, s4
	s_mul_i32 s4, s4, 28
	s_lshl_b32 s3, s3, 2
	s_add_i32 s4, s4, s3
	s_add_i32 s95, s4, s1
	v_writelane_b32 v255, s95, 20
	s_mov_b32 s12, s85
	s_mov_b32 s0, s62
	s_mov_b64 s[16:17], s[86:87]
	s_waitcnt lgkmcnt(0)
	v_mbcnt_lo_u32_b32 v0, s0, 0
	v_mbcnt_hi_u32_b32 v196, s0, v0
	v_lshl_add_u32 v197, s12, 6, v196
	v_cmp_eq_u32_e64 s[14:15], 0, v197
	s_barrier
	s_and_saveexec_b64 s[2:3], s[14:15]
	s_cbranch_execz .LBB0_1363
	s_lshl_b32 s64, s58, 4
	s_lshl_b64 s[0:1], s[64:65], 2
	s_add_u32 s0, s72, s0
	s_addc_u32 s1, s73, s1
	global_load_dwordx4 v[0:3], v209, s[0:1] offset:272
	global_load_dwordx4 v[4:7], v209, s[0:1] offset:256
	v_readlane_b32 s0, v253, 16
	v_mov_b32_e32 v12, v209
	s_waitcnt vmcnt(1)
	v_add_u32_e32 v0, 0xff, v0
	s_waitcnt vmcnt(0)
	v_add_u32_e32 v4, 0xff, v4
	v_add_u32_e32 v5, 0xff, v5
	v_ashrrev_i32_e32 v8, 31, v4
	v_add_u32_sdwa v4, v4, v8 dst_sel:DWORD dst_unused:UNUSED_PAD src0_sel:DWORD src1_sel:BYTE_3
	v_ashrrev_i32_e32 v8, 31, v5
	v_add_u32_sdwa v5, v5, v8 dst_sel:DWORD dst_unused:UNUSED_PAD src0_sel:DWORD src1_sel:BYTE_3
	v_ashrrev_i32_e32 v9, 8, v4
	v_ashrrev_i32_e32 v5, 8, v5
	v_add_u32_e32 v10, v5, v9
	v_lshlrev_b32_e32 v14, 8, v10
	v_and_b32_e32 v13, 0xffffff00, v4
	v_mov_b32_e32 v4, s0
	ds_write_b96 v4, v[12:14]
	v_add_u32_e32 v4, 0xff, v6
	v_ashrrev_i32_e32 v5, 31, v4
	v_add_u32_sdwa v4, v4, v5 dst_sel:DWORD dst_unused:UNUSED_PAD src0_sel:DWORD src1_sel:BYTE_3
	v_add_u32_e32 v5, 0xff, v7
	v_ashrrev_i32_e32 v6, 31, v5
	v_ashrrev_i32_e32 v4, 8, v4
	v_add_u32_sdwa v5, v5, v6 dst_sel:DWORD dst_unused:UNUSED_PAD src0_sel:DWORD src1_sel:BYTE_3
	v_readlane_b32 s0, v253, 17
	v_ashrrev_i32_e32 v5, 8, v5
	v_add_u32_e32 v11, v4, v10
	v_mov_b32_e32 v8, v209
	v_mov_b32_e32 v4, s0
	ds_write_b128 v4, v[8:11]
	v_add_u32_e32 v4, v5, v11
	v_readlane_b32 s0, v253, 18
	v_lshlrev_b32_e32 v5, 8, v11
	v_lshlrev_b32_e32 v6, 8, v4
	v_mov_b32_e32 v7, s0
	ds_write2_b32 v7, v5, v6 offset1:1
	v_ashrrev_i32_e32 v5, 31, v0
	v_add_u32_e32 v1, 0xff, v1
	v_add_u32_sdwa v0, v0, v5 dst_sel:DWORD dst_unused:UNUSED_PAD src0_sel:DWORD src1_sel:BYTE_3
	v_ashrrev_i32_e32 v5, 31, v1
	v_ashrrev_i32_e32 v0, 8, v0
	v_add_u32_sdwa v1, v1, v5 dst_sel:DWORD dst_unused:UNUSED_PAD src0_sel:DWORD src1_sel:BYTE_3
	v_ashrrev_i32_e32 v1, 8, v1
	v_add_u32_e32 v5, v0, v4
	v_add_u32_e32 v6, v1, v5
	v_readlane_b32 s0, v253, 19
	v_lshlrev_b32_e32 v0, 8, v5
	v_lshlrev_b32_e32 v1, 8, v6
	v_mov_b32_e32 v7, s0
	ds_write2_b32 v7, v0, v1 offset1:1
	v_add_u32_e32 v0, 0xff, v2
	v_ashrrev_i32_e32 v1, 31, v0
	v_add_u32_sdwa v0, v0, v1 dst_sel:DWORD dst_unused:UNUSED_PAD src0_sel:DWORD src1_sel:BYTE_3
	v_ashrrev_i32_e32 v0, 8, v0
	v_readlane_b32 s0, v253, 20
	v_add_u32_e32 v7, v0, v6
	v_lshlrev_b32_e32 v0, 8, v7
	v_mov_b32_e32 v1, s0
	v_readlane_b32 s0, v253, 21
	ds_write_b128 v1, v[4:7]
	s_nop 0
	v_mov_b32_e32 v1, s0
	ds_write_b32 v1, v0
	v_add_u32_e32 v0, 0xff, v3
	v_ashrrev_i32_e32 v1, 31, v0
	v_add_u32_sdwa v0, v0, v1 dst_sel:DWORD dst_unused:UNUSED_PAD src0_sel:DWORD src1_sel:BYTE_3
	v_ashrrev_i32_e32 v0, 8, v0
	v_readlane_b32 s0, v253, 22
	v_add_u32_e32 v0, v0, v7
	s_nop 0
	v_mov_b32_e32 v1, s0
	ds_write_b32 v1, v0

.LBB0_1415:
	s_add_i32 s95, s36, 1
	s_and_b64 vcc, exec, s[20:21]
	s_cbranch_vccz .LBB0_1420
	s_cmp_ge_i32 s95, s51
	s_cbranch_scc0 .LBB0_1423
	s_sub_i32 s4, s95, s51
	v_readlane_b32 s5, v254, 5
	s_cmp_ge_i32 s4, s5
	s_cbranch_scc0 .LBB0_1481
	s_sub_i32 s22, s4, s5
	v_readlane_b32 s4, v254, 7
	s_cmp_ge_i32 s22, s4
	s_cbranch_scc0 .LBB0_1482
	v_readlane_b32 s6, v253, 32
	v_readlane_b32 s7, v253, 33
	s_load_dword s5, s[6:7], 0x148
	s_sub_i32 s4, s22, s4
	s_mov_b32 s37, 1
	s_mov_b32 s15, 4
	s_waitcnt lgkmcnt(0)
	s_mul_i32 s4, s4, s5
	v_readlane_b32 s5, v255, 20
	s_add_i32 s14, s4, s5
	v_readlane_b32 s4, v254, 1
	s_cmp_lt_i32 s14, s4
	s_cselect_b64 s[4:5], -1, 0
	s_cbranch_execz .LBB0_1483
	s_branch .LBB0_1484

.LBB0_1423:
	s_mov_b64 s[4:5], 0
	s_cbranch_execz .LBB0_1425
	v_readlane_b32 s4, v253, 32
	v_readlane_b32 s5, v253, 33
	s_load_dword s4, s[4:5], 0x148
	v_readlane_b32 s5, v255, 20
	s_mov_b32 s37, 0
	s_mov_b32 s15, 28
	s_waitcnt lgkmcnt(0)
	s_mul_i32 s4, s95, s4
	s_add_i32 s14, s4, s5
	s_mov_b64 s[4:5], -1

.LBB0_1426:
	v_readlane_b32 s4, v253, 32
	v_readlane_b32 s5, v253, 33
	s_load_dword s4, s[4:5], 0x148
	v_readlane_b32 s5, v255, 20
	s_waitcnt lgkmcnt(0)
	s_mul_i32 s4, s95, s4
	s_add_i32 s14, s4, s5
	s_cmp_lt_i32 s14, s49
	s_cselect_b64 s[4:5], -1, 0
	s_cmp_ge_i32 s14, s49
	s_cbranch_scc0 .LBB0_1428
	s_sub_i32 s14, s14, s49
	v_readlane_b32 s4, v254, 1
	s_cmp_lt_i32 s14, s4
	s_mov_b32 s37, 1
	s_mov_b32 s15, 4
	s_cselect_b64 s[4:5], -1, 0
	s_and_b64 vcc, exec, s[4:5]
	s_cbranch_vccz .LBB0_1429
	s_branch .LBB0_1422

.LBB0_1490:
	v_readlane_b32 s95, v253, 34
	v_readlane_b32 s96, v253, 36
	s_cmp_lg_u32 s59, 1
	v_readlane_b32 s97, v253, 37
	s_cbranch_scc1 .LBB0_1503
	s_cmp_lt_i32 s12, 7
	s_mul_i32 s0, s12, 0x4800
	v_lshlrev_b32_e32 v0, 2, v196
	s_cselect_b32 s0, s0, 0x21000
	v_and_b32_e32 v4, 28, v0
	v_lshrrev_b32_e32 v0, 1, v196
	s_add_i32 s4, s0, 0
	v_lshrrev_b32_e32 v2, 3, v196
	v_and_b32_e32 v3, 31, v196
	v_and_b32_e32 v0, 48, v0
	s_add_u32 s0, s18, 0x12400000
	v_lshl_add_u32 v5, v4, 2, s4
	v_mul_u32_u24_e32 v6, 0x90, v2
	v_lshl_add_u32 v7, v3, 2, s4
	v_mul_u32_u24_e32 v8, 0x90, v0
	v_cmp_eq_u32_e64 s[2:3], 0, v196
	s_addc_u32 s1, s19, 0
	v_mov_b32_e32 v1, v209
	v_lshlrev_b32_e32 v208, 2, v4
	v_add_u32_e32 v4, v5, v6
	v_add_u32_e32 v5, v7, v8
	s_branch .LBB0_1494
